# baseline (speedup 1.0000x reference)
.LBB2_3:
	s_add_i32 s19, s15, s19
	s_cmpk_lt_i32 s19, 0x61b
	s_cselect_b64 s[8:9], -1, 0
	s_cmpk_gt_i32 s19, 0x61a
	s_cselect_b64 s[0:1], -1, 0
	s_setprio 0
	s_cmpk_ge_i32 s19, 0x61b
	s_cbranch_scc1 .Lpl_g1
	s_setprio 1
	s_cmpk_ge_i32 s19, 0x41b
	s_cbranch_scc1 .Lpl_g1
	s_setprio 2
	s_cmpk_ge_i32 s19, 0x21b
	s_cbranch_scc1 .Lpl_g1
	s_setprio 3
.Lpl_g1:
	s_and_b64 vcc, exec, s[0:1]
	s_cbranch_vccnz .LBB2_5
	v_add_u32_e32 v60, s14, v215
	v_min_i32_e32 v34, 0xc34f, v60
	v_add_u32_e32 v36, 8, v60
	v_add_u32_e32 v58, 16, v60
	v_add_u32_e32 v60, 24, v60
	v_min_i32_e32 v36, 0xc34f, v36
	v_min_i32_e32 v58, 0xc34f, v58
	v_min_i32_e32 v60, 0xc34f, v60
	v_ashrrev_i32_e32 v35, 31, v34
	v_ashrrev_i32_e32 v37, 31, v36
	v_ashrrev_i32_e32 v59, 31, v58
	v_ashrrev_i32_e32 v61, 31, v60
	v_lshlrev_b64 v[34:35], 9, v[34:35]
	v_lshlrev_b64 v[36:37], 9, v[36:37]
	v_lshlrev_b64 v[58:59], 9, v[58:59]
	v_lshlrev_b64 v[60:61], 9, v[60:61]
	v_lshl_add_u64 v[34:35], v[210:211], 0, v[34:35]
	v_lshl_add_u64 v[38:39], v[210:211], 0, v[36:37]
	v_lshl_add_u64 v[58:59], v[210:211], 0, v[58:59]
	v_lshl_add_u64 v[70:71], v[210:211], 0, v[60:61]
	global_load_dwordx4 v[34:37], v[34:35], off nt
	s_nop 0
	global_load_dwordx4 v[38:41], v[38:39], off nt
	s_nop 0
	global_load_dwordx4 v[58:61], v[58:59], off nt
	s_nop 0
	global_load_dwordx4 v[70:73], v[70:71], off nt

.LBB3_3:
	s_add_i32 s2, s12, s2
	s_cmpk_lt_i32 s2, 0x61b
	s_cselect_b64 s[4:5], -1, 0
	s_cmpk_gt_i32 s2, 0x61a
	s_cselect_b64 s[0:1], -1, 0
	s_setprio 0
	s_cmpk_ge_i32 s2, 0x61b
	s_cbranch_scc1 .Lpl_g2
	s_setprio 1
	s_cmpk_ge_i32 s2, 0x41b
	s_cbranch_scc1 .Lpl_g2
	s_setprio 2
	s_cmpk_ge_i32 s2, 0x21b
	s_cbranch_scc1 .Lpl_g2
	s_setprio 3
.Lpl_g2:
	s_and_b64 vcc, exec, s[0:1]
	s_cbranch_vccnz .LBB3_5
	v_add_u32_e32 v156, s3, v218
	v_min_i32_e32 v146, 0xc34f, v156
	v_add_u32_e32 v148, 8, v156
	v_add_u32_e32 v154, 16, v156
	v_add_u32_e32 v156, 24, v156
	v_min_i32_e32 v148, 0xc34f, v148
	v_min_i32_e32 v154, 0xc34f, v154
	v_min_i32_e32 v156, 0xc34f, v156
	v_ashrrev_i32_e32 v147, 31, v146
	v_ashrrev_i32_e32 v149, 31, v148
	v_ashrrev_i32_e32 v155, 31, v154
	v_ashrrev_i32_e32 v157, 31, v156
	v_lshlrev_b64 v[146:147], 9, v[146:147]
	v_lshlrev_b64 v[148:149], 9, v[148:149]
	v_lshlrev_b64 v[154:155], 9, v[154:155]
	v_lshlrev_b64 v[156:157], 9, v[156:157]
	v_lshl_add_u64 v[146:147], v[212:213], 0, v[146:147]
	v_lshl_add_u64 v[150:151], v[212:213], 0, v[148:149]
	v_lshl_add_u64 v[154:155], v[212:213], 0, v[154:155]
	v_lshl_add_u64 v[158:159], v[212:213], 0, v[156:157]
	global_load_dwordx4 v[146:149], v[146:147], off nt
	s_nop 0
	global_load_dwordx4 v[150:153], v[150:151], off nt
	s_nop 0
	global_load_dwordx4 v[154:157], v[154:155], off nt
	s_nop 0
	global_load_dwordx4 v[158:161], v[158:159], off nt
